# speedup vs baseline: 1.0096x; 1.0096x over previous
_Z6k_gemmPKfS0_PK15HIP_vector_typeIjLj4EEPDF16_PKh:
	s_load_dwordx4 s[20:23], s[0:1], 0x0
	s_load_dwordx4 s[4:7], s[0:1], 0x10
	s_load_dwordx2 s[38:39], s[0:1], 0x20
	v_readfirstlane_b32 s8, v0
	v_and_b32_e32 v1, 63, v0
	s_nop 3
	s_lshr_b32 s8, s8, 6
	s_and_b32 s40, s2, 7
	s_lshr_b32 s41, s2, 3
	s_mul_i32 s18, s40, 0x187
	s_add_u32 s19, s18, 0x187
	s_min_u32 s19, s19, 0xc35
	s_sub_u32 s33, s19, s18
	s_sub_u32 s33, s33, 0x180
	s_lshl_b32 s33, s33, 2
	s_cmp_lt_u32 s41, s33
	s_cselect_b32 s44, 7, 6
	s_lshr_b32 s45, s41, 2
	s_add_u32 s45, s45, s18
	s_add_u32 s45, s45, 0x180
	s_lshl_b32 s45, s45, 4
	s_and_b32 s46, s41, 3
	s_lshl_b32 s46, s46, 2
	s_add_u32 s47, s45, s46
	s_mul_i32 s45, s47, 0x4b0
	s_lshl_b32 s46, s47, 8
	s_add_i32 s18, s18, s41
	s_cmp_eq_u32 s8, 0
	s_cselect_b32 s9, s44, 6
	s_add_i32 s11, s44, 4
	s_lshl_b32 s18, s18, 4
	s_lshl_b32 s19, s8, 2
	s_add_i32 s33, s18, s19
	s_mul_i32 s12, s33, 0x4b0
	s_lshl_b32 s32, s18, 8
	s_sub_u32 s32, s32, 0x100000
	s_mov_b32 s10, 0
	v_lshl_add_u32 v253, v1, 10, s33
	v_mov_b32_e32 v254, s47
	v_cmp_eq_u32_e32 vcc, 6, v1
	s_nop 1
	v_cndmask_b32_e32 v253, v253, v254, vcc
	v_mov_b32_e32 v247, 0
	v_cmp_gt_i32_e32 vcc, s9, v1
	s_mov_b32 s18, 0xc350
	v_cmp_gt_i32_e64 s[36:37], s18, v253
	s_and_b64 vcc, vcc, s[36:37]
	s_waitcnt lgkmcnt(0)
	s_and_saveexec_b64 s[36:37], vcc
	global_load_dword v247, v253, s[38:39]
	s_mov_b64 exec, s[36:37]
	s_mov_b32 s24, s22
	s_and_b32 s25, s23, 0xffff
	s_mov_b32 s26, 0x3938700
	s_mov_b32 s27, 0x20000
	s_and_b32 s21, s21, 0xffff
	s_mov_b32 s22, 0x3938700
	s_mov_b32 s23, 0x20000
	s_mov_b32 s28, s6
	s_and_b32 s29, s7, 0xffff
	s_mov_b32 s30, 0xc35000
	s_mov_b32 s31, 0x20000
	v_lshlrev_b32_e32 v238, 4, v1
	v_mul_u32_u24_e32 v253, 0x1746, v1
	v_lshrrev_b32_e32 v253, 16, v253
	v_min_u32_e32 v253, 3, v253
	v_mul_u32_u24_e32 v254, 11, v253
	v_sub_u32_e32 v254, v1, v254
	v_lshlrev_b32_e32 v240, 3, v253
	v_mul_u32_u24_e32 v249, 0x4b0, v253
	v_lshl_add_u32 v249, v254, 4, v249
	v_add_u32_e32 v249, 0x400, v249
	v_mov_b32_e32 v255, 0x80000000
	v_cmp_gt_u32_e64 s[34:35], 44, v1
	s_nop 1
	v_cndmask_b32_e64 v239, v255, v249, s[34:35]
	v_lshl_add_u32 v250, s8, 2, v253
	v_mul_u32_u24_e32 v250, 0x4e0, v250
	v_lshl_add_u32 v250, v254, 3, v250
	v_add_u32_e32 v242, 0x200, v250
	s_mul_i32 s18, s8, 0x1380
	v_lshl_add_u32 v241, v1, 3, s18
	v_and_b32_e32 v249, 15, v1
	v_lshrrev_b32_e32 v250, 4, v1
	v_mul_u32_u24_e32 v243, 0x4e0, v249
	v_lshl_add_u32 v243, v250, 4, v243
	v_mul_u32_u24_e32 v244, 0x440, v250
	v_lshl_add_u32 v244, v249, 1, v244
	s_lshl_b32 s18, s8, 6
	s_add_i32 s18, s18, 39936
	v_add_u32_e32 v244, s18, v244
	v_lshrrev_b32_e32 v249, 4, v0
	v_and_b32_e32 v250, 15, v0
	v_mul_u32_u24_e32 v245, 0x110, v249
	v_lshl_add_u32 v245, v250, 4, v245
	v_add_u32_e32 v245, 39936, v245
	v_lshlrev_b32_e32 v246, 8, v249
	v_lshl_add_u32 v246, v250, 4, v246
	s_lshl_b32 s18, s8, 12
	s_add_i32 s18, s18, 48640
	v_lshl_add_u32 v248, v1, 4, s18
	v_cmp_gt_u32_e32 vcc, 32, v0
	s_and_saveexec_b64 s[36:37], vcc
	v_mul_u32_u24_e32 v251, 0x4e00, v249
	v_mul_u32_u24_e32 v252, 0x4e0, v250
	v_add_u32_e32 v254, v251, v252
	v_mov_b32_e32 v250, 0
	v_mov_b32_e32 v251, 0
	v_mov_b32_e32 v252, 0
	v_mov_b32_e32 v253, 0
	ds_write_b128 v254, v[250:253] offset:1200
	s_mov_b64 exec, s[36:37]
	s_lshl_b32 s18, s8, 11
	v_lshl_add_u32 v253, v1, 4, s18
	v_add_u32_e32 v254, 0x22000, v253
	global_load_dwordx4 v[178:181], v254, s[4:5]
	global_load_dwordx4 v[182:185], v254, s[4:5] offset:1024
	v_add_u32_e32 v254, 0x2000, v254
	global_load_dwordx4 v[186:189], v254, s[4:5]
	global_load_dwordx4 v[190:193], v254, s[4:5] offset:1024
	v_mov_b32_e32 v236, v253
	s_waitcnt vmcnt(4)
	v_readlane_b32 s13, v247, s10
	s_add_u32 s14, s12, 0x4b0
	s_add_u32 s15, s12, 0x960
	s_add_u32 s16, s12, 0xe10
	s_nop 1
	s_and_b32 s18, s13, 0xff
	s_cmp_eq_u32 s18, 1
	s_cselect_b32 s42, s12, 0x80000000
	s_and_b32 s18, s13, 0xff00
	s_cmp_eq_u32 s18, 0x100
	s_cselect_b32 s14, s14, 0x80000000
	s_and_b32 s18, s13, 0xff0000
	s_cmp_eq_u32 s18, 0x10000
	s_cselect_b32 s15, s15, 0x80000000
	s_and_b32 s18, s13, 0xff000000
	s_cmp_eq_u32 s18, 0x1000000
	s_cselect_b32 s16, s16, 0x80000000
	v_lshrrev_b32_e64 v249, v240, s13
	v_and_b32_e32 v249, 0xff, v249
	v_cmp_eq_u32_e32 vcc, 1, v249
	s_nop 1
	v_cndmask_b32_e32 v254, v255, v239, vcc
	buffer_load_dwordx4 v[138:141], v238, s[20:23], s42 offen nt
	buffer_load_dwordx4 v[142:145], v238, s[24:27], s42 offen nt
	buffer_load_dwordx4 v[146:149], v238, s[20:23], s14 offen nt
	buffer_load_dwordx4 v[150:153], v238, s[24:27], s14 offen nt
	buffer_load_dwordx4 v[154:157], v238, s[20:23], s15 offen nt
	buffer_load_dwordx4 v[158:161], v238, s[24:27], s15 offen nt
	buffer_load_dwordx4 v[162:165], v238, s[20:23], s16 offen nt
	buffer_load_dwordx4 v[166:169], v238, s[24:27], s16 offen nt
	buffer_load_dwordx4 v[170:173], v254, s[20:23], s12 offen nt
	buffer_load_dwordx4 v[174:177], v254, s[24:27], s12 offen nt
	s_add_u32 s12, s12, 0x12c000
	s_add_u32 s32, s32, 0x40000
	s_mov_b32 s19, 0x80000000
	buffer_store_dwordx4 v[226:229], v246, s[28:31], s19 offen sc1
	s_mov_b32 s10, 1
	global_load_dwordx4 v[2:5], v236, s[4:5]
	global_load_dwordx4 v[6:9], v236, s[4:5] offset:1024
	v_add_u32_e32 v236, 0x2000, v236
	global_load_dwordx4 v[10:13], v236, s[4:5]
	global_load_dwordx4 v[14:17], v236, s[4:5] offset:1024
	v_add_u32_e32 v236, 0x2000, v236
	global_load_dwordx4 v[18:21], v236, s[4:5]
	global_load_dwordx4 v[22:25], v236, s[4:5] offset:1024
	v_add_u32_e32 v236, 0x2000, v236
	global_load_dwordx4 v[26:29], v236, s[4:5]
	global_load_dwordx4 v[30:33], v236, s[4:5] offset:1024
	v_add_u32_e32 v236, 0x2000, v236
	global_load_dwordx4 v[34:37], v236, s[4:5]
	global_load_dwordx4 v[38:41], v236, s[4:5] offset:1024
	v_add_u32_e32 v236, 0x2000, v236
	global_load_dwordx4 v[42:45], v236, s[4:5]
	global_load_dwordx4 v[46:49], v236, s[4:5] offset:1024
	v_add_u32_e32 v236, 0x2000, v236
	global_load_dwordx4 v[50:53], v236, s[4:5]
	global_load_dwordx4 v[54:57], v236, s[4:5] offset:1024
	v_add_u32_e32 v236, 0x2000, v236
	global_load_dwordx4 v[58:61], v236, s[4:5]
	global_load_dwordx4 v[62:65], v236, s[4:5] offset:1024
	v_add_u32_e32 v236, 0x2000, v236
	global_load_dwordx4 v[66:69], v236, s[4:5]
	global_load_dwordx4 v[70:73], v236, s[4:5] offset:1024
	v_add_u32_e32 v236, 0x2000, v236
	global_load_dwordx4 v[74:77], v236, s[4:5]
	global_load_dwordx4 v[78:81], v236, s[4:5] offset:1024
	v_add_u32_e32 v236, 0x2000, v236
	global_load_dwordx4 v[82:85], v236, s[4:5]
	global_load_dwordx4 v[86:89], v236, s[4:5] offset:1024
	v_add_u32_e32 v236, 0x2000, v236
	global_load_dwordx4 v[90:93], v236, s[4:5]
	global_load_dwordx4 v[94:97], v236, s[4:5] offset:1024
	v_add_u32_e32 v236, 0x2000, v236
	global_load_dwordx4 v[98:101], v236, s[4:5]
	global_load_dwordx4 v[102:105], v236, s[4:5] offset:1024
	v_add_u32_e32 v236, 0x2000, v236
	global_load_dwordx4 v[106:109], v236, s[4:5]
	global_load_dwordx4 v[110:113], v236, s[4:5] offset:1024
	v_add_u32_e32 v236, 0x2000, v236
	global_load_dwordx4 v[114:117], v236, s[4:5]
	global_load_dwordx4 v[118:121], v236, s[4:5] offset:1024
	v_add_u32_e32 v236, 0x2000, v236
	global_load_dwordx4 v[122:125], v236, s[4:5]
	global_load_dwordx4 v[126:129], v236, s[4:5] offset:1024
	v_add_u32_e32 v236, 0x2000, v236
	global_load_dwordx4 v[130:133], v236, s[4:5]
	global_load_dwordx4 v[134:137], v236, s[4:5] offset:1024
	s_waitcnt vmcnt(45)
	ds_write_b128 v248, v[178:181]
	ds_write_b128 v248, v[182:185] offset:1024
	ds_write_b128 v248, v[186:189] offset:2048
	ds_write_b128 v248, v[190:193] offset:3072
	s_waitcnt lgkmcnt(0)
	s_barrier
	s_branch .Lg_half1

.Lg_s3skip0:
	s_cmp_eq_u32 s10, 10
	s_cselect_b32 s32, s46, s32
	s_sub_u32 s18, s10, 4
	s_cmp_lt_u32 s18, s9
	s_cselect_b32 s19, s32, 0x80000000
	ds_read_b128 v[226:229], v245 offset:0
	s_add_u32 s32, s32, 0x40000
	s_waitcnt lgkmcnt(0)
	buffer_store_dwordx4 v[226:229], v246, s[28:31], s19 offen sc1
	s_barrier
	s_add_u32 s10, s10, 1
	s_cmp_ge_u32 s10, s11
	s_cbranch_scc1 .Lg_end

.Lg_s3skip1:
	s_cmp_eq_u32 s10, 10
	s_cselect_b32 s32, s46, s32
	s_sub_u32 s18, s10, 4
	s_cmp_lt_u32 s18, s9
	s_cselect_b32 s19, s32, 0x80000000
	ds_read_b128 v[226:229], v245 offset:4352
	s_add_u32 s32, s32, 0x40000
	s_waitcnt lgkmcnt(0)
	buffer_store_dwordx4 v[226:229], v246, s[28:31], s19 offen sc1
	s_barrier
	s_add_u32 s10, s10, 1
	s_cmp_lt_u32 s10, s11
	s_cbranch_scc1 .Lg_top
